# speedup vs baseline: 1.0056x; 1.0052x over previous
.LBB1_12:
	s_mov_b32 s0, s44
	s_add_i32 s44, s44, 1
	s_cmp_ge_u32 s44, s42
	s_cselect_b64 s[22:23], -1, 0
	s_cmp_lt_u32 s44, s42
	s_cselect_b32 s2, s44, s0
	s_waitcnt vmcnt(0)
	s_sleep 4
	s_lshl_b32 s0, s2, 4
	s_mov_b32 s1, s17
	s_mov_b32 m0, s43
	ds_read_b128 v[76:79], v119 offset:32768
	ds_read_b128 v[80:83], v119 offset:36864
	ds_read_b128 v[84:87], v120 offset:32768
	ds_read_b128 v[88:91], v120 offset:36864
	ds_read_b128 v[92:95], v121
	ds_read_b128 v[96:99], v121 offset:4096
	ds_read_b128 v[128:131], v122
	ds_read_b128 v[132:135], v122 offset:4096
	ds_read_b128 v[72:75], v123
	s_waitcnt lgkmcnt(0)
	v_lshl_add_u64 v[70:71], s[0:1], 2, v[2:3]
	global_load_lds_dword v[70:71], off
	ds_read_b128 v[156:159], v115
	ds_read_b128 v[160:163], v115 offset:1024
	ds_read_b128 v[164:167], v115 offset:2048
	v_cvt_pk_bf16_f32 v136, v76, v77
	v_cvt_pk_bf16_f32 v137, v78, v79
	v_cvt_pk_bf16_f32 v138, v84, v85
	v_cvt_pk_bf16_f32 v139, v86, v87
	v_cvt_pk_bf16_f32 v140, v92, v93
	v_cvt_pk_bf16_f32 v141, v94, v95
	v_cvt_pk_bf16_f32 v142, v128, v129
	v_cvt_pk_bf16_f32 v143, v130, v131
	v_cvt_pk_bf16_f32 v144, v80, v81
	v_cvt_pk_bf16_f32 v145, v82, v83
	v_cvt_pk_bf16_f32 v146, v88, v89
	v_cvt_pk_bf16_f32 v147, v90, v91
	v_cvt_pk_bf16_f32 v128, v96, v97
	v_cvt_pk_bf16_f32 v129, v98, v99
	v_cvt_pk_bf16_f32 v130, v132, v133
	v_cvt_pk_bf16_f32 v131, v134, v135
	s_lshl_b32 s0, s2, 13
	s_cmp_lt_u32 s44, s42
	s_cselect_b32 s0, s0, 0x1e848000
	ds_read_b128 v[132:135], v115 offset:3072
	s_waitcnt lgkmcnt(3)
	v_mfma_f32_16x16x32_bf16 v[148:151], v[136:139], v[156:159], v[36:39]
	ds_read_b128 v[156:159], v115 offset:4096
	s_waitcnt lgkmcnt(3)
	v_mfma_f32_16x16x32_bf16 v[152:155], v[136:139], v[160:163], v[40:43]
	ds_read_b128 v[160:163], v115 offset:5120
	s_waitcnt lgkmcnt(3)
	v_mfma_f32_16x16x32_bf16 v[96:99], v[136:139], v[164:167], v[44:47]
	ds_read_b128 v[164:167], v115 offset:6144
	s_waitcnt lgkmcnt(3)
	v_mfma_f32_16x16x32_bf16 v[92:95], v[136:139], v[132:135], v[48:51]
	s_mov_b32 m0, s47
	s_nop 0
	buffer_load_dwordx4 v113, s[12:15], s0 offen nt lds
	ds_read_b128 v[132:135], v115 offset:7168
	s_waitcnt lgkmcnt(3)
	v_mfma_f32_16x16x32_bf16 v[88:91], v[136:139], v[156:159], v[52:55]
	ds_read_b128 v[156:159], v115 offset:8192
	s_waitcnt lgkmcnt(3)
	v_mfma_f32_16x16x32_bf16 v[84:87], v[136:139], v[160:163], v[56:59]
	ds_read_b128 v[160:163], v115 offset:9216
	s_waitcnt lgkmcnt(3)
	v_mfma_f32_16x16x32_bf16 v[80:83], v[136:139], v[164:167], v[60:63]
	ds_read_b128 v[164:167], v115 offset:10240
	s_waitcnt lgkmcnt(3)
	v_mfma_f32_16x16x32_bf16 v[76:79], v[136:139], v[132:135], v[64:67]
	s_or_b32 s1, s0, 0x800
	s_mov_b32 m0, s48
	s_nop 0
	buffer_load_dwordx4 v113, s[12:15], s1 offen nt lds
	ds_read_b128 v[132:135], v115 offset:11264
	s_waitcnt lgkmcnt(3)
	v_mfma_f32_16x16x32_bf16 v[148:151], v[140:143], v[156:159], v[148:151]
	ds_read_b128 v[156:159], v115 offset:12288
	s_waitcnt lgkmcnt(3)
	v_mfma_f32_16x16x32_bf16 v[152:155], v[140:143], v[160:163], v[152:155]
	ds_read_b128 v[160:163], v115 offset:13312
	s_waitcnt lgkmcnt(3)
	v_mfma_f32_16x16x32_bf16 v[96:99], v[140:143], v[164:167], v[96:99]
	ds_read_b128 v[164:167], v115 offset:14336
	s_waitcnt lgkmcnt(3)
	v_mfma_f32_16x16x32_bf16 v[92:95], v[140:143], v[132:135], v[92:95]
	s_or_b32 s1, s0, 0x1000
	s_mov_b32 m0, s49
	s_nop 0
	buffer_load_dwordx4 v113, s[12:15], s1 offen nt lds
	ds_read_b128 v[132:135], v115 offset:15360
	s_waitcnt lgkmcnt(3)
	v_mfma_f32_16x16x32_bf16 v[88:91], v[140:143], v[156:159], v[88:91]
	ds_read_b128 v[156:159], v115 offset:16384
	s_waitcnt lgkmcnt(3)
	v_mfma_f32_16x16x32_bf16 v[84:87], v[140:143], v[160:163], v[84:87]
	ds_read_b128 v[160:163], v115 offset:17408
	s_waitcnt lgkmcnt(3)
	v_mfma_f32_16x16x32_bf16 v[80:83], v[140:143], v[164:167], v[80:83]
	ds_read_b128 v[164:167], v115 offset:18432
	s_waitcnt lgkmcnt(3)
	v_mfma_f32_16x16x32_bf16 v[76:79], v[140:143], v[132:135], v[76:79]
	s_or_b32 s1, s0, 0x1800
	s_mov_b32 m0, s50
	s_nop 0
	buffer_load_dwordx4 v113, s[12:15], s1 offen nt lds
	ds_read_b128 v[132:135], v115 offset:19456
	s_waitcnt lgkmcnt(3)
	v_mfma_f32_16x16x32_bf16 v[148:151], v[144:147], v[156:159], v[148:151]
	ds_read_b128 v[156:159], v115 offset:20480
	s_waitcnt lgkmcnt(3)
	v_mfma_f32_16x16x32_bf16 v[152:155], v[144:147], v[160:163], v[152:155]
	ds_read_b128 v[160:163], v115 offset:21504
	s_waitcnt lgkmcnt(3)
	v_mfma_f32_16x16x32_bf16 v[96:99], v[144:147], v[164:167], v[96:99]
	ds_read_b128 v[164:167], v115 offset:22528
	s_waitcnt lgkmcnt(3)
	v_mfma_f32_16x16x32_bf16 v[92:95], v[144:147], v[132:135], v[92:95]
	s_or_b32 s1, s0, 0x100
	s_mov_b32 m0, s51
	s_nop 0
	buffer_load_dwordx4 v113, s[12:15], s1 offen nt lds
	ds_read_b128 v[132:135], v115 offset:23552
	s_waitcnt lgkmcnt(3)
	v_mfma_f32_16x16x32_bf16 v[88:91], v[144:147], v[156:159], v[88:91]
	ds_read_b128 v[156:159], v115 offset:24576
	s_waitcnt lgkmcnt(3)
	v_mfma_f32_16x16x32_bf16 v[84:87], v[144:147], v[160:163], v[84:87]
	ds_read_b128 v[160:163], v115 offset:25600
	s_waitcnt lgkmcnt(3)
	v_mfma_f32_16x16x32_bf16 v[80:83], v[144:147], v[164:167], v[80:83]
	ds_read_b128 v[164:167], v115 offset:26624
	s_waitcnt lgkmcnt(3)
	v_mfma_f32_16x16x32_bf16 v[76:79], v[144:147], v[132:135], v[76:79]
	s_or_b32 s1, s0, 0x900
	s_mov_b32 m0, s52
	s_nop 0
	buffer_load_dwordx4 v113, s[12:15], s1 offen nt lds
	ds_read_b128 v[132:135], v115 offset:27648
	s_waitcnt lgkmcnt(3)
	v_mfma_f32_16x16x32_bf16 v[148:151], v[128:131], v[156:159], v[148:151]
	ds_read_b128 v[156:159], v115 offset:28672
	s_waitcnt lgkmcnt(3)
	v_mfma_f32_16x16x32_bf16 v[152:155], v[128:131], v[160:163], v[152:155]
	ds_read_b128 v[160:163], v115 offset:29696
	s_waitcnt lgkmcnt(3)
	v_mfma_f32_16x16x32_bf16 v[96:99], v[128:131], v[164:167], v[96:99]
	ds_read_b128 v[164:167], v115 offset:30720
	s_waitcnt lgkmcnt(3)
	v_mfma_f32_16x16x32_bf16 v[92:95], v[128:131], v[132:135], v[92:95]
	s_or_b32 s1, s0, 0x1100
	s_mov_b32 m0, s53
	s_nop 0
	buffer_load_dwordx4 v113, s[12:15], s1 offen nt lds
	ds_read_b128 v[132:135], v115 offset:31744
	s_waitcnt lgkmcnt(3)
	v_mfma_f32_16x16x32_bf16 v[88:91], v[128:131], v[156:159], v[88:91]
	s_waitcnt lgkmcnt(2)
	v_mfma_f32_16x16x32_bf16 v[84:87], v[128:131], v[160:163], v[84:87]
	s_waitcnt lgkmcnt(1)
	v_mfma_f32_16x16x32_bf16 v[80:83], v[128:131], v[164:167], v[80:83]
	s_waitcnt lgkmcnt(0)
	v_mfma_f32_16x16x32_bf16 v[76:79], v[128:131], v[132:135], v[76:79]
	s_or_b32 s1, s0, 0x1900
	s_mov_b32 m0, s54
	s_nop 0
	buffer_load_dwordx4 v113, s[12:15], s1 offen nt lds
	ds_read2_b32 v[136:137], v114 offset0:128 offset1:144
	ds_read2_b32 v[138:139], v125 offset1:16
	ds_read2_b32 v[140:141], v114 offset0:160 offset1:176
	ds_read2_b32 v[142:143], v125 offset0:32 offset1:48
	ds_read2_b32 v[144:145], v114 offset0:192 offset1:208
	ds_read2_b32 v[146:147], v125 offset0:64 offset1:80
	ds_read2_b32 v[156:157], v114 offset0:224 offset1:240
	ds_read2_b32 v[158:159], v125 offset0:96 offset1:112
	v_fma_f32 v70, v149, v149, 0
	v_fmac_f32_e32 v70, v153, v153
	v_fmac_f32_e32 v70, v97, v97
	v_fmac_f32_e32 v70, v93, v93
	v_fmac_f32_e32 v70, v89, v89
	v_fmac_f32_e32 v70, v85, v85
	v_fmac_f32_e32 v70, v81, v81
	v_fmac_f32_e32 v70, v77, v77
	v_fma_f32 v68, v148, v148, 0
	v_fmac_f32_e32 v68, v152, v152
	v_add_f32_dpp v70, v70, v70 quad_perm:[1,0,3,2] row_mask:0xf bank_mask:0xf bound_ctrl:1
	v_fmac_f32_e32 v68, v96, v96
	v_fmac_f32_e32 v68, v92, v92
	v_add_f32_dpp v70, v70, v70 quad_perm:[2,3,0,1] row_mask:0xf bank_mask:0xf bound_ctrl:1
	v_fmac_f32_e32 v68, v88, v88
	v_fmac_f32_e32 v68, v84, v84
	v_add_f32_dpp v70, v70, v70 row_half_mirror row_mask:0xf bank_mask:0xf bound_ctrl:1
	v_fmac_f32_e32 v68, v80, v80
	v_fmac_f32_e32 v68, v76, v76
	v_add_f32_dpp v70, v70, v70 row_mirror row_mask:0xf bank_mask:0xf bound_ctrl:1
	v_fmamk_f32 v70, v70, 0x3c000000, v124
	v_rsq_f32_e32 v127, v70
	v_fma_f32 v70, v150, v150, 0
	v_fmac_f32_e32 v70, v154, v154
	v_fmac_f32_e32 v70, v98, v98
	v_fmac_f32_e32 v70, v94, v94
	v_fmac_f32_e32 v70, v90, v90
	v_fmac_f32_e32 v70, v86, v86
	v_fmac_f32_e32 v70, v82, v82
	v_fmac_f32_e32 v70, v78, v78
	v_add_f32_dpp v68, v68, v68 quad_perm:[1,0,3,2] row_mask:0xf bank_mask:0xf bound_ctrl:1
	v_mul_f32_e32 v131, v127, v149
	v_add_f32_dpp v70, v70, v70 quad_perm:[1,0,3,2] row_mask:0xf bank_mask:0xf bound_ctrl:1
	v_add_f32_dpp v68, v68, v68 quad_perm:[2,3,0,1] row_mask:0xf bank_mask:0xf bound_ctrl:1
	v_mul_f32_e32 v81, v127, v81
	v_add_f32_dpp v70, v70, v70 quad_perm:[2,3,0,1] row_mask:0xf bank_mask:0xf bound_ctrl:1
	v_add_f32_dpp v68, v68, v68 row_half_mirror row_mask:0xf bank_mask:0xf bound_ctrl:1
	v_cmp_gt_u32_e64 s[0:1], s55, v72
	v_add_f32_dpp v70, v70, v70 row_half_mirror row_mask:0xf bank_mask:0xf bound_ctrl:1
	v_add_f32_dpp v68, v68, v68 row_mirror row_mask:0xf bank_mask:0xf bound_ctrl:1
	v_fmamk_f32 v68, v68, 0x3c000000, v124
	v_add_f32_dpp v70, v70, v70 row_mirror row_mask:0xf bank_mask:0xf bound_ctrl:1
	v_fmamk_f32 v70, v70, 0x3c000000, v124
	v_rsq_f32_e32 v130, v70
	v_fma_f32 v70, v151, v151, 0
	v_fmac_f32_e32 v70, v155, v155
	v_fmac_f32_e32 v70, v99, v99
	v_fmac_f32_e32 v70, v95, v95
	v_fmac_f32_e32 v70, v91, v91
	v_fmac_f32_e32 v70, v87, v87
	v_fmac_f32_e32 v70, v83, v83
	v_fmac_f32_e32 v70, v79, v79
	v_rsq_f32_e32 v68, v68
	v_mul_f32_e32 v98, v130, v98
	v_add_f32_dpp v70, v70, v70 quad_perm:[1,0,3,2] row_mask:0xf bank_mask:0xf bound_ctrl:1
	v_mul_f32_e32 v90, v130, v90
	v_mul_f32_e32 v111, v68, v148
	v_add_f32_dpp v110, v70, v70 quad_perm:[2,3,0,1] row_mask:0xf bank_mask:0xf bound_ctrl:1
	s_nop 1
	v_add_f32_dpp v110, v110, v110 row_half_mirror row_mask:0xf bank_mask:0xf bound_ctrl:1
	v_mul_f32_e32 v96, v68, v96
	v_mul_f32_e32 v92, v68, v92
	v_add_f32_dpp v110, v110, v110 row_mirror row_mask:0xf bank_mask:0xf bound_ctrl:1
	v_fmamk_f32 v110, v110, 0x3c000000, v124
	s_waitcnt lgkmcnt(0)
	v_fma_f32 v111, v111, v136, v138
	v_fma_f32 v131, v131, v136, v138
	v_exp_f32_e32 v111, v111
	v_exp_f32_e32 v131, v131
	v_rsq_f32_e32 v132, v110
	v_mul_f32_e32 v88, v68, v88
	v_add_f32_e32 v110, 1.0, v111
	v_add_f32_e32 v111, 1.0, v131
	v_mul_f32_e32 v131, v130, v150
	v_mul_f32_e32 v133, v132, v151
	v_fma_f32 v131, v131, v136, v138
	v_fma_f32 v70, v133, v136, v138
	v_exp_f32_e32 v131, v131
	v_exp_f32_e32 v70, v70
	v_rcp_f32_e32 v110, v110
	v_rcp_f32_e32 v111, v111
	v_add_f32_e32 v128, 1.0, v131
	v_add_f32_e32 v70, 1.0, v70
	v_rcp_f32_e32 v128, v128
	v_rcp_f32_e32 v70, v70
	v_mul_f32_e32 v131, v68, v152
	v_fma_f32 v131, v131, v137, v139
	v_cvt_pk_bf16_f32 v110, v110, v111
	v_cvt_pk_bf16_f32 v111, v128, v70
	v_mul_f32_e32 v128, v127, v153
	v_exp_f32_e32 v131, v131
	v_fma_f32 v128, v128, v137, v139
	v_exp_f32_e32 v128, v128
	v_mul_f32_e32 v99, v132, v99
	v_add_f32_e32 v70, 1.0, v131
	v_rcp_f32_e32 v133, v70
	v_add_f32_e32 v70, 1.0, v128
	v_mul_f32_e32 v131, v130, v154
	v_rcp_f32_e32 v134, v70
	v_mul_f32_e32 v70, v132, v155
	v_fma_f32 v131, v131, v137, v139
	v_fma_f32 v129, v70, v137, v139
	v_exp_f32_e32 v135, v129
	v_exp_f32_e32 v131, v131
	v_mul_f32_e32 v91, v132, v91
	v_add_f32_e32 v135, 1.0, v135
	v_rcp_f32_e32 v135, v135
	v_fma_f32 v96, v96, v140, v142
	v_exp_f32_e32 v136, v96
	v_mul_f32_e32 v96, v127, v97
	v_fma_f32 v96, v96, v140, v142
	v_exp_f32_e32 v97, v96
	v_fma_f32 v98, v98, v140, v142
	v_fma_f32 v70, v99, v140, v142
	v_exp_f32_e32 v98, v98
	v_exp_f32_e32 v70, v70
	v_add_f32_e32 v97, 1.0, v97
	v_cvt_pk_bf16_f32 v96, v133, v134
	v_add_f32_e32 v133, 1.0, v136
	v_rcp_f32_e32 v99, v97
	v_add_f32_e32 v97, 1.0, v98
	v_add_f32_e32 v70, 1.0, v70
	v_fma_f32 v92, v92, v141, v143
	v_rcp_f32_e32 v133, v133
	v_rcp_f32_e32 v128, v97
	v_rcp_f32_e32 v70, v70
	v_exp_f32_e32 v92, v92
	v_cvt_pk_bf16_f32 v98, v133, v99
	v_add_f32_e32 v131, 1.0, v131
	v_cvt_pk_bf16_f32 v99, v128, v70
	v_add_f32_e32 v70, 1.0, v92
	v_mul_f32_e32 v92, v127, v93
	v_fma_f32 v92, v92, v141, v143
	v_exp_f32_e32 v92, v92
	v_mul_f32_e32 v93, v130, v94
	v_fma_f32 v93, v93, v141, v143
	v_rcp_f32_e32 v131, v131
	v_exp_f32_e32 v93, v93
	v_rcp_f32_e32 v94, v70
	v_add_f32_e32 v70, 1.0, v92
	v_rcp_f32_e32 v128, v70
	v_mul_f32_e32 v70, v132, v95
	v_cvt_pk_bf16_f32 v97, v131, v135
	v_add_f32_e32 v131, 1.0, v93
	v_fma_f32 v129, v70, v141, v143
	v_exp_f32_e32 v95, v129
	v_rcp_f32_e32 v129, v131
	v_mul_f32_e32 v84, v68, v84
	v_mul_f32_e32 v80, v68, v80
	v_fma_f32 v88, v88, v144, v146
	v_exp_f32_e32 v131, v88
	v_mul_f32_e32 v88, v127, v89
	v_fma_f32 v88, v88, v144, v146
	v_exp_f32_e32 v89, v88
	v_fma_f32 v90, v90, v144, v146
	v_fma_f32 v70, v91, v144, v146
	v_exp_f32_e32 v90, v90
	v_exp_f32_e32 v70, v70
	v_add_f32_e32 v89, 1.0, v89
	v_cvt_pk_bf16_f32 v88, v94, v128
	v_add_f32_e32 v94, 1.0, v131
	v_rcp_f32_e32 v91, v89
	v_add_f32_e32 v89, 1.0, v90
	v_add_f32_e32 v70, 1.0, v70
	v_fma_f32 v84, v84, v145, v147
	v_rcp_f32_e32 v94, v94
	v_rcp_f32_e32 v92, v89
	v_rcp_f32_e32 v70, v70
	v_exp_f32_e32 v84, v84
	v_cvt_pk_bf16_f32 v90, v94, v91
	v_mul_f32_e32 v68, v68, v76
	v_cvt_pk_bf16_f32 v91, v92, v70
	v_add_f32_e32 v70, 1.0, v84
	v_mul_f32_e32 v84, v127, v85
	v_fma_f32 v84, v84, v145, v147
	v_mul_f32_e32 v85, v130, v86
	v_exp_f32_e32 v84, v84
	v_fma_f32 v85, v85, v145, v147
	v_exp_f32_e32 v85, v85
	v_rcp_f32_e32 v92, v70
	v_add_f32_e32 v70, 1.0, v84
	v_rcp_f32_e32 v84, v70
	v_add_f32_e32 v70, 1.0, v85
	v_mul_f32_e32 v85, v132, v87
	v_fma_f32 v93, v85, v145, v147
	v_exp_f32_e32 v85, v93
	v_rcp_f32_e32 v93, v70
	v_mul_f32_e32 v76, v127, v77
	v_mul_f32_e32 v82, v130, v82
	v_mul_f32_e32 v83, v132, v83
	v_mul_f32_e32 v77, v130, v78
	v_fma_f32 v76, v76, v157, v159
	v_mul_f32_e32 v78, v132, v79
	v_fma_f32 v80, v80, v156, v158
	v_fma_f32 v81, v81, v156, v158
	v_fma_f32 v82, v82, v156, v158
	v_fma_f32 v70, v83, v156, v158
	v_fma_f32 v68, v68, v157, v159
	v_exp_f32_e32 v76, v76
	v_fma_f32 v77, v77, v157, v159
	v_fma_f32 v87, v78, v157, v159
	v_exp_f32_e32 v82, v82
	v_exp_f32_e32 v70, v70
	v_exp_f32_e32 v68, v68
	v_exp_f32_e32 v77, v77
	v_exp_f32_e32 v71, v87
	v_add_f32_e32 v76, 1.0, v76
	v_add_f32_e32 v82, 1.0, v82
	v_add_f32_e32 v70, 1.0, v70
	v_add_f32_e32 v68, 1.0, v68
	v_rcp_f32_e32 v78, v76
	v_add_f32_e32 v76, 1.0, v77
	v_add_f32_e32 v71, 1.0, v71
	v_rcp_f32_e32 v82, v82
	v_rcp_f32_e32 v70, v70
	v_rcp_f32_e32 v68, v68
	v_rcp_f32_e32 v79, v76
	v_rcp_f32_e32 v71, v71
	v_exp_f32_e32 v80, v80
	v_exp_f32_e32 v81, v81
	v_cvt_pk_bf16_f32 v77, v82, v70
	v_cvt_pk_bf16_f32 v78, v68, v78
	v_cvt_pk_bf16_f32 v79, v79, v71
	v_subrev_u32_e32 v68, s16, v72
	v_subrev_u32_e32 v70, s16, v73
	v_subrev_u32_e32 v71, s16, v74
	v_add_f32_e32 v95, 1.0, v95
	v_add_f32_e32 v85, 1.0, v85
	v_add_f32_e32 v80, 1.0, v80
	v_add_f32_e32 v81, 1.0, v81
	v_max3_u32 v68, v68, v70, v71
	v_subrev_u32_e32 v70, s16, v75
	v_rcp_f32_e32 v95, v95
	v_rcp_f32_e32 v85, v85
	v_rcp_f32_e32 v80, v80
	v_rcp_f32_e32 v81, v81
	v_max_u32_e32 v68, v68, v70
	v_cmp_gt_u32_e32 vcc, 16, v68
	s_cmp_eq_u64 vcc, -1
	s_cselect_b64 s[24:25], -1, 0
	s_cmp_lg_u64 vcc, -1
	v_cvt_pk_bf16_f32 v89, v129, v95
	v_cvt_pk_bf16_f32 v84, v92, v84
	v_cvt_pk_bf16_f32 v85, v93, v85
	v_cvt_pk_bf16_f32 v76, v80, v81
	s_cselect_b64 s[26:27], -1, 0
	v_cmp_gt_u32_e64 s[2:3], s55, v73
	v_cmp_gt_u32_e64 s[4:5], s55, v74
	v_cmp_gt_u32_e64 s[6:7], s55, v75
	s_mov_b32 s8, 0
	s_branch .LBB1_14
